# kpre + QK(t+1) rotated to the tail of step t ahead of the end-of-step barrier (score init + 8 QK MFMAs on prefetched K registers), QK(0) in the pre-loop
# baseline (speedup 1.0000x reference)
; #define LAS __attribute__((address_space(3)))
; #define MFMA32(a, b, c) __builtin_amdgcn_mfma_f32_32x32x16_bf16((a), (b), (c), 0, 0, 0)
; DI int at_v_rd_base(int lane) { return ((lane & 3) << 3) | (((lane >> 2) & 3) << 6) | (((lane >> 4) & 1) << 5) | (((lane >> 5) & 1) << 8); }
;     __device__ __forceinline__ void init(const void* A_, const void* B_, int lda_, int ldb_, int M, unsigned mask_, int G_, int c_) { A = (const char*)A_; B = (const char*)B_; lda = lda_; ldb = ldb_; nM = M / BM; mask = mask_; nN = __builtin_popcount(mask_); nwg = nM * nN; G = G_; c = c_; }
; template <int KS> DI void at_qk(f32x16& p0, f32x16& p1, LAS const unsigned char* Kt, int mapB, const bf16x8 (&qr)[8], float init, int r32, int hi) {
; #pragma unroll
;     for (int i = 0; i < 16; ++i) { p0[i] = init; p1[i] = init; }
;     bf16x8 kb[KS][2];
; #pragma unroll
;     for (int d0 = 0; d0 < KS; ++d0) { const int cb = mapB + (d0 * 16 + hi * 8) * 2;
;         kb[d0][0] = *(const LAS bf16x8*)(Kt + AT_KSWZ(r32, cb)); kb[d0][1] = *(const LAS bf16x8*)(Kt + AT_KSWZ(32 + r32, cb)); }
;     __builtin_amdgcn_sched_barrier(0);
; #pragma unroll
;     for (int d0 = 0; d0 < KS; ++d0) { p0 = MFMA32(kb[d0][0], qr[d0], p0); p1 = MFMA32(kb[d0][1], qr[d0], p1); }
; DI void attn_unit_diff(const Ctx& C, int l, int b, int h, int j) {
;     ...
;     f32x16 o[4], ol = {}; float m_run = 0.f; bool first = true;
; #pragma unroll
;     for (int d0 = 0; d0 < 4; ++d0) o[d0] = f32x16{};
;     const bf16x8 ones = {16256, 16256, 16256, 16256, 16256, 16256, 16256, 16256};
;     asm volatile("s_waitcnt vmcnt(0) lgkmcnt(0)\n\ts_barrier" ::: "memory");
;     const float cfar = tabl[0];
;     const int vrd = at_v_rd_base(lane);
;     for (int sd = 0; sd < nt; ++sd) {
;         const int slot = sd % 3;
;         const bool staged = sd + 2 < nt;
;         if (staged) at_stage1(C.lds, projb, kcolB, vcolB, sd + 2, (sd + 2) % 3, wid, lb0, lb1);
;         if (sd <= cw) {
;             LAS const unsigned char* Kt = C.lds + slot * 32768;
;             const int vb = (int)(size_t)(Kt + 16384) + vrd;
;             const bool nearb = (sd * 64 + 63 - q0w) > -305;
;             LAS const float* tabp = tabl + (sd * 64 - qpos + TABB_OFF + 4 * hi);
;             f32x16 p0, p1;
;             at_qk<KS>(p0, p1, Kt, g * 128, qr, (nearb ? 0.f : cfar) - m_run, r32, hi);
.LBB0_785:
	s_or_b64 exec, exec, s[38:39]
	s_add_i32 s50, 0, 0x20000
	s_lshr_b32 s28, s97, 4
	s_lshl_b32 s66, s49, 1
	v_readlane_b32 s38, v252, 22
	s_waitcnt vmcnt(0) lgkmcnt(0)
	s_barrier
	v_mov_b32_e32 v4, s50
	s_and_b32 s28, s28, 7
	s_or_b32 s67, s66, s38
	s_waitcnt lgkmcnt(0)
	ds_read_b32 v158, v4
	v_and_b32_e32 v4, 24, v8
	v_and_b32_e32 v7, 0x100, v8
	v_lshlrev_b32_e32 v8, 4, v156
	v_readlane_b32 s38, v252, 26
	s_lshl_b32 s28, s28, 8
	v_lshlrev_b32_e32 v145, 4, v154
	v_add_u32_e32 v9, s38, v8
	v_readlane_b32 s38, v252, 23
	v_lshlrev_b32_e32 v11, 4, v155
	v_lshlrev_b32_e32 v15, 2, v154
	s_add_i32 s88, s55, 0xfffffe90
	s_add_i32 s38, s38, s52
	s_add_i32 s91, 0, 0x4000
	s_add_i32 s52, s48, s28
	v_mov_b32_e32 v3, v1
	v_and_b32_e32 v5, 0xc0, v145
	v_lshlrev_b32_e32 v6, 1, v154
	v_lshlrev_b32_e32 v10, 8, v155
	v_and_b32_e32 v11, 0x70, v11
	v_add_u32_e32 v14, 0x60, v9
	v_xor_b32_e32 v157, 0x80, v15
	v_add_lshl_u32 v15, s38, v155, 2
	s_add_u32 s38, s96, s42
	v_and_b32_e32 v6, 32, v6
	v_add_u32_e32 v12, 32, v9
	v_add_u32_e32 v13, 64, v9
	v_sub_u32_e32 v159, v8, v15
	v_add3_u32 v5, v7, s91, v5
	v_xad_u32 v164, v14, v11, v10
	v_lshl_add_u64 v[2:3], s[42:43], 0, v[2:3]
	s_addc_u32 s39, s89, s43
	v_mov_b32_e32 v14, v1
	v_mov_b32_e32 v15, v1
	v_add3_u32 v160, v5, v6, v4
	v_xad_u32 v161, v9, v11, v10
	v_xad_u32 v162, v12, v11, v10
	v_xad_u32 v163, v13, v11, v10
	v_lshl_add_u64 v[146:147], s[70:71], 0, v[2:3]
	v_lshl_add_u64 v[148:149], s[72:73], 0, v[2:3]
	v_lshl_add_u64 v[150:151], s[38:39], 0, v[0:1]
	s_lshl_b32 s95, s49, 16
	v_mov_b32_e32 v0, v1
	v_mov_b32_e32 v2, v1
	v_mov_b32_e32 v3, v1
	v_mov_b32_e32 v4, v1
	v_mov_b32_e32 v5, v1
	v_mov_b32_e32 v6, v1
	v_mov_b32_e32 v7, v1
	v_mov_b32_e32 v8, v1
	v_mov_b32_e32 v9, v1
	v_mov_b32_e32 v10, v1
	v_mov_b32_e32 v11, v1
	v_mov_b32_e32 v12, v1
	v_mov_b32_e32 v13, v1
	v_mov_b64_e32 v[78:79], v[14:15]
	v_mov_b64_e32 v[62:63], v[14:15]
	v_mov_b64_e32 v[46:47], v[14:15]
	v_mov_b64_e32 v[30:31], v[14:15]
	v_mov_b64_e32 v[94:95], v[14:15]
	s_mov_b32 s79, 2
	s_add_i32 s95, s95, 0x10000
	s_mov_b32 s48, 0
	v_mov_b32_e32 v165, 0
	s_mov_b64 s[38:39], -1
	s_mov_b32 s49, 0
	v_mov_b64_e32 v[76:77], v[12:13]
	v_mov_b64_e32 v[74:75], v[10:11]
	v_mov_b64_e32 v[72:73], v[8:9]
	v_mov_b64_e32 v[70:71], v[6:7]
	v_mov_b64_e32 v[68:69], v[4:5]
	v_mov_b64_e32 v[66:67], v[2:3]
	v_mov_b64_e32 v[64:65], v[0:1]
	v_mov_b64_e32 v[60:61], v[12:13]
	v_mov_b64_e32 v[58:59], v[10:11]
	v_mov_b64_e32 v[56:57], v[8:9]
	v_mov_b64_e32 v[54:55], v[6:7]
	v_mov_b64_e32 v[52:53], v[4:5]
	v_mov_b64_e32 v[50:51], v[2:3]
	v_mov_b64_e32 v[48:49], v[0:1]
	v_mov_b64_e32 v[44:45], v[12:13]
	v_mov_b64_e32 v[42:43], v[10:11]
	v_mov_b64_e32 v[40:41], v[8:9]
	v_mov_b64_e32 v[38:39], v[6:7]
	v_mov_b64_e32 v[36:37], v[4:5]
	v_mov_b64_e32 v[34:35], v[2:3]
	v_mov_b64_e32 v[32:33], v[0:1]
	v_mov_b64_e32 v[28:29], v[12:13]
	v_mov_b64_e32 v[26:27], v[10:11]
	v_mov_b64_e32 v[24:25], v[8:9]
	v_mov_b64_e32 v[22:23], v[6:7]
	v_mov_b64_e32 v[20:21], v[4:5]
	v_mov_b64_e32 v[18:19], v[2:3]
	v_mov_b64_e32 v[16:17], v[0:1]
	v_mov_b64_e32 v[92:93], v[12:13]
	v_mov_b64_e32 v[90:91], v[10:11]
	v_mov_b64_e32 v[88:89], v[8:9]
	v_mov_b64_e32 v[86:87], v[6:7]
	v_mov_b64_e32 v[84:85], v[4:5]
	v_mov_b64_e32 v[82:83], v[2:3]
	v_mov_b64_e32 v[80:81], v[0:1]
	s_mov_b32 s94, 0
	s_waitcnt vmcnt(0)
	s_mul_hi_u32 s57, s79, 0xaaaaaaab
	s_lshr_b32 s57, s57, 1
	s_mul_i32 s57, s57, 0x18000
	s_sub_i32 s58, s60, s57
	s_sub_i32 s59, s61, s57
	s_add_i32 s58, s49, s58
	v_lshl_add_u64 v[2:3], v[150:151], 0, s[52:53]
	s_sub_i32 s80, s4, s57
	s_add_i32 m0, s90, s58
	v_lshl_add_u64 v[4:5], v[2:3], 0, s[36:37]
	s_add_i32 s58, s49, s59
	s_sub_i32 s57, s5, s57
	global_load_lds_dwordx4 v[4:5], off
	v_lshl_add_u64 v[4:5], v[148:149], 0, s[52:53]
	s_add_i32 m0, s90, s58
	s_add_i32 s58, s49, s80
	global_load_lds_dwordx4 v[4:5], off
	v_lshl_add_u64 v[2:3], v[2:3], 0, s[24:25]
	s_add_i32 m0, s90, s58
	s_add_i32 s57, s49, s57
	global_load_lds_dwordx4 v[2:3], off
	v_lshl_add_u64 v[2:3], v[146:147], 0, s[52:53]
	s_add_i32 m0, s90, s57
	s_nop 0
	global_load_lds_dwordx4 v[2:3], off
	v_lshl_add_u64 v[146:147], v[146:147], 0, s[68:69]
	v_lshl_add_u64 v[148:149], v[148:149], 0, s[68:69]
	v_lshl_add_u64 v[150:151], v[150:151], 0, s[68:69]
	ds_read_b128 v[186:189], v161
	ds_read_b128 v[190:193], v161 offset:8192
	ds_read_b128 v[202:205], v162
	ds_read_b128 v[206:209], v162 offset:8192
	ds_read_b128 v[210:213], v163
	ds_read_b128 v[214:217], v163 offset:8192
	ds_read_b128 v[218:221], v164
	ds_read_b128 v[222:225], v164 offset:8192
	s_cmp_le_u32 s48, s88
	s_cselect_b64 vcc, -1, 0
	s_waitcnt lgkmcnt(0)
	v_cndmask_b32_e32 v2, 0, v158, vcc
	v_sub_f32_e32 v96, v2, v165
	v_mov_b32_e32 v97, v96
	v_mov_b32_e32 v98, v96
	v_mov_b32_e32 v99, v96
	v_mov_b32_e32 v100, v96
	v_mov_b32_e32 v101, v96
	v_mov_b32_e32 v102, v96
	v_mov_b32_e32 v103, v96
	v_mov_b32_e32 v104, v96
	v_mov_b32_e32 v105, v96
	v_mov_b32_e32 v106, v96
	v_mov_b32_e32 v107, v96
	v_mov_b32_e32 v108, v96
	v_mov_b32_e32 v109, v96
	v_mov_b32_e32 v110, v96
	v_mov_b32_e32 v111, v96
	s_waitcnt lgkmcnt(0)
	s_nop 0
	v_mfma_f32_32x32x16_bf16 v[112:127], v[186:189], v[128:131], v[96:111]
	v_mfma_f32_32x32x16_bf16 v[96:111], v[190:193], v[128:131], v[96:111]
	v_mfma_f32_32x32x16_bf16 v[112:127], v[202:205], v[132:135], v[112:127]
	v_mfma_f32_32x32x16_bf16 v[96:111], v[206:209], v[132:135], v[96:111]
	v_mfma_f32_32x32x16_bf16 v[112:127], v[210:213], v[136:139], v[112:127]
	v_mfma_f32_32x32x16_bf16 v[96:111], v[214:217], v[136:139], v[96:111]
	v_mfma_f32_32x32x16_bf16 v[112:127], v[218:221], v[140:143], v[112:127]
	v_mfma_f32_32x32x16_bf16 v[96:111], v[222:225], v[140:143], v[96:111]
	s_branch .LBB0_787

; #define LAS __attribute__((address_space(3)))
; DI float at_softmax(f32x16& p0, f32x16& p1, float& m_run, bool first, bool nearb, LAS const float* tabp, int lane) {
;     if (nearb) {
; #pragma unroll
;         for (int i = 0; i < 16; ++i) { p0[i] += tabp[8 * (i >> 2) + (i & 3)]; p1[i] += tabp[32 + 8 * (i >> 2) + (i & 3)]; }
;     }
;     float mx = p0[0];
; #pragma unroll
;     for (int i = 1; i < 16; ++i) mx = fmaxf(mx, p0[i]);
; #pragma unroll
;     for (int i = 0; i < 16; ++i) mx = fmaxf(mx, p1[i]);
; DI void attn_unit_diff(const Ctx& C, int l, int b, int h, int j) {
;     ...
;         if (sd <= cw) {
;             LAS const unsigned char* Kt = C.lds + slot * 32768;
;             const int vb = (int)(size_t)(Kt + 16384) + vrd;
;             const bool nearb = (sd * 64 + 63 - q0w) > -305;
;             LAS const float* tabp = tabl + (sd * 64 - qpos + TABB_OFF + 4 * hi);
;             f32x16 p0, p1;
;             at_qk<KS>(p0, p1, Kt, g * 128, qr, (nearb ? 0.f : cfar) - m_run, r32, hi);
;             const float alpha = at_softmax(p0, p1, m_run, first, nearb, tabp, lane);
.LBB0_792:
	s_lshr_b32 s57, s94, 2
	s_lshl_b32 s57, s57, 17
	s_add_i32 s100, s94, 1
	s_and_b32 s100, s100, 3
	s_lshl_b32 s100, s100, 15
	s_add_i32 s58, s49, 0
	s_cmp_le_u32 s48, s88
	s_cselect_b64 vcc, -1, 0
	s_and_b64 vcc, exec, vcc
	s_cbranch_vccnz .LBB0_794
	v_add_u32_e32 v0, 0, v159
	v_add_u32_e32 v2, 0x207fc, v0
	v_add_u32_e32 v4, 0x2087c, v0
	ds_read2_b32 v[2:3], v2 offset1:1
	ds_read2_b32 v[4:5], v4 offset1:1
	v_add_u32_e32 v6, 0x20804, v0
	v_add_u32_e32 v8, 0x20884, v0
	v_add_u32_e32 v10, 0x2081c, v0
	v_add_u32_e32 v12, 0x2089c, v0
	v_add_u32_e32 v14, 0x20824, v0
	v_add_u32_e32 v166, 0x208a4, v0
	v_add_u32_e32 v168, 0x2083c, v0
	v_add_u32_e32 v170, 0x208bc, v0
	v_add_u32_e32 v172, 0x20844, v0
	v_add_u32_e32 v174, 0x208c4, v0
	v_add_u32_e32 v176, 0x2085c, v0
	v_add_u32_e32 v178, 0x208dc, v0
	v_add_u32_e32 v180, 0x20864, v0
	v_add_u32_e32 v0, 0x208e4, v0
	ds_read2_b32 v[6:7], v6 offset1:1
	ds_read2_b32 v[8:9], v8 offset1:1
	ds_read2_b32 v[10:11], v10 offset1:1
	ds_read2_b32 v[12:13], v12 offset1:1
	ds_read2_b32 v[14:15], v14 offset1:1
	ds_read2_b32 v[166:167], v166 offset1:1
	ds_read2_b32 v[168:169], v168 offset1:1
	ds_read2_b32 v[170:171], v170 offset1:1
	ds_read2_b32 v[172:173], v172 offset1:1
	ds_read2_b32 v[174:175], v174 offset1:1
	ds_read2_b32 v[176:177], v176 offset1:1
	ds_read2_b32 v[178:179], v178 offset1:1
	ds_read2_b32 v[180:181], v180 offset1:1
	s_waitcnt lgkmcnt(0)
	v_pk_add_f32 v[112:113], v[112:113], v[2:3]
	ds_read2_b32 v[2:3], v0 offset1:1
	v_pk_add_f32 v[124:125], v[124:125], v[176:177]
	v_pk_add_f32 v[122:123], v[122:123], v[172:173]
	v_pk_add_f32 v[126:127], v[126:127], v[180:181]
	v_pk_add_f32 v[120:121], v[120:121], v[168:169]
	v_pk_add_f32 v[118:119], v[118:119], v[14:15]
	v_pk_add_f32 v[116:117], v[116:117], v[10:11]
	v_pk_add_f32 v[114:115], v[114:115], v[6:7]
	s_waitcnt lgkmcnt(0)
	v_pk_add_f32 v[110:111], v[110:111], v[2:3]
	v_pk_add_f32 v[108:109], v[108:109], v[178:179]
	v_pk_add_f32 v[106:107], v[106:107], v[174:175]
	v_pk_add_f32 v[104:105], v[104:105], v[170:171]
	v_pk_add_f32 v[102:103], v[102:103], v[166:167]
	v_pk_add_f32 v[100:101], v[100:101], v[12:13]
	v_pk_add_f32 v[98:99], v[98:99], v[8:9]
	v_pk_add_f32 v[96:97], v[96:97], v[4:5]
.LBB0_794:
	s_nop 0
	v_max_f32_e32 v0, v113, v113
	v_max_f32_e32 v2, v112, v112
	v_max_f32_e32 v0, v2, v0
	v_max3_f32 v0, v0, v114, v115
	v_max3_f32 v0, v0, v116, v117
	v_max3_f32 v0, v0, v118, v119
	v_max3_f32 v0, v0, v120, v121
	v_max3_f32 v0, v0, v122, v123
	v_max3_f32 v0, v0, v124, v125
	v_max3_f32 v0, v0, v126, v127
	v_max3_f32 v0, v0, v96, v97
	v_max3_f32 v0, v0, v98, v99
	v_max3_f32 v0, v0, v100, v101
	v_max3_f32 v0, v0, v102, v103
	v_max3_f32 v0, v0, v104, v105
	v_max3_f32 v0, v0, v106, v107
	s_xor_b64 s[58:59], s[38:39], -1
	v_max3_f32 v0, v0, v108, v109
	v_max3_f32 v2, v0, v110, v111
	s_and_b64 vcc, exec, s[58:59]
	s_cbranch_vccz .LBB0_796
	s_mov_b32 s58, 0x41000000
	v_cmp_ge_f32_e32 vcc, s58, v2
	s_cmp_lg_u64 vcc, exec
	s_cselect_b64 s[58:59], -1, 0
	s_cbranch_execz .LBB0_797
	s_branch .LBB0_798

; #define MFMA32(a, b, c) __builtin_amdgcn_mfma_f32_32x32x16_bf16((a), (b), (c), 0, 0, 0)
; DI float at_softmax(f32x16& p0, f32x16& p1, float& m_run, bool first, bool nearb, LAS const float* tabp, int lane) {
;     ...
;     for (int i = 0; i < 16; ++i) p0[i] = __builtin_amdgcn_exp2f(p0[i]);
; #pragma unroll
;     for (int i = 0; i < 16; ++i) p1[i] = __builtin_amdgcn_exp2f(p1[i]);
;     return alpha;
; }
; DI bf16x8 at_pack(const f32x16& p, int s8) {
;     u32x4 w; w.x = at_cvtpk(p[s8], p[s8 + 1]); w.y = at_cvtpk(p[s8 + 2], p[s8 + 3]); w.z = at_cvtpk(p[s8 + 4], p[s8 + 5]); w.w = at_cvtpk(p[s8 + 6], p[s8 + 7]);
;     return __builtin_bit_cast(bf16x8, w);
; }
; template <int D0> DI void at_pv_block(f32x16 (&o)[4], int vb, const bf16x8 (&pf)[4]) {
;     const s16x4 l0 = at_tr_read<D0 * 512 + 0 * 4096>(vb), h0 = at_tr_read<D0 * 512 + 0 * 4096 + 2048>(vb), l1 = at_tr_read<D0 * 512 + 1 * 4096>(vb), h1 = at_tr_read<D0 * 512 + 1 * 4096 + 2048>(vb);
;     const s16x4 l2 = at_tr_read<D0 * 512 + 2 * 4096>(vb), h2 = at_tr_read<D0 * 512 + 2 * 4096 + 2048>(vb), l3 = at_tr_read<D0 * 512 + 3 * 4096>(vb), h3 = at_tr_read<D0 * 512 + 3 * 4096 + 2048>(vb);
;     asm volatile("s_waitcnt lgkmcnt(0)" ::: "memory"); __builtin_amdgcn_sched_barrier(0);
;     ...
;     o[D0] = MFMA32(AT_PK(l0, h0), pf[0], o[D0]); o[D0] = MFMA32(AT_PK(l1, h1), pf[1], o[D0]); o[D0] = MFMA32(AT_PK(l2, h2), pf[2], o[D0]); o[D0] = MFMA32(AT_PK(l3, h3), pf[3], o[D0]);
; DI void attn_unit_diff(const Ctx& C, int l, int b, int h, int j) {
;     ...
;             at_qk<KS>(p0, p1, Kt, g * 128, qr, (nearb ? 0.f : cfar) - m_run, r32, hi);
;             const float alpha = at_softmax(p0, p1, m_run, first, nearb, tabp, lane);
;             first = false;
;             if (__any(alpha != 1.f)) {
;                 ol[0] *= alpha;
; #pragma unroll
;                 for (int d0 = 0; d0 < 4; ++d0)
; #pragma unroll
;                     for (int i = 0; i < 16; ++i) o[d0][i] *= alpha;
;             }
;             bf16x8 pf[4];
;             pf[0] = at_pack(p0, 0); pf[1] = at_pack(p0, 8); pf[2] = at_pack(p1, 0); pf[3] = at_pack(p1, 8);
;             ol = MFMA32(ones, pf[0], ol); ol = MFMA32(ones, pf[1], ol); ol = MFMA32(ones, pf[2], ol); ol = MFMA32(ones, pf[3], ol);
;             at_pv_block<0>(o, vb, pf); at_pv_block<1>(o, vb, pf); at_pv_block<2>(o, vb, pf); at_pv_block<3>(o, vb, pf);
.LBB0_801:
	v_subrev_u32_e32 v87, s57, v160
	v_add_u32_e32 v87, s49, v87
	ds_read_b64_tr_b16 v[170:171], v87 offset:0x0
	ds_read_b64_tr_b16 v[172:173], v87 offset:0x800
	ds_read_b64_tr_b16 v[174:175], v87 offset:0x200
	ds_read_b64_tr_b16 v[176:177], v87 offset:0xa00
	ds_read_b64_tr_b16 v[178:179], v87 offset:0x400
	ds_read_b64_tr_b16 v[180:181], v87 offset:0xc00
	ds_read_b64_tr_b16 v[182:183], v87 offset:0x600
	ds_read_b64_tr_b16 v[184:185], v87 offset:0xe00
	v_exp_f32_e32 v112, v112
	v_exp_f32_e32 v113, v113
	v_exp_f32_e32 v114, v114
	v_exp_f32_e32 v115, v115
	v_exp_f32_e32 v116, v116
	v_exp_f32_e32 v117, v117
	v_exp_f32_e32 v118, v118
	v_exp_f32_e32 v119, v119
	v_cvt_pk_bf16_f32 v2, v112, v113
	v_cvt_pk_bf16_f32 v3, v114, v115
	v_cvt_pk_bf16_f32 v4, v116, v117
	v_cvt_pk_bf16_f32 v5, v118, v119
	v_add_f32_e32 v81, v112, v113
	v_add_f32_e32 v82, v114, v115
	v_add_f32_e32 v83, v116, v117
	v_add_f32_e32 v84, v118, v119
	v_add_f32_e32 v81, v81, v82
	v_add_f32_e32 v83, v83, v84
	v_add_f32_e32 v81, v81, v83
	v_add_f32_e32 v80, v80, v81
	s_waitcnt lgkmcnt(0)
	ds_read_b64_tr_b16 v[112:113], v87 offset:0x1000
	ds_read_b64_tr_b16 v[114:115], v87 offset:0x1800
	ds_read_b64_tr_b16 v[116:117], v87 offset:0x1200
	ds_read_b64_tr_b16 v[118:119], v87 offset:0x1a00
	ds_read_b64_tr_b16 v[88:89], v87 offset:0x1400
	ds_read_b64_tr_b16 v[90:91], v87 offset:0x1c00
	ds_read_b64_tr_b16 v[92:93], v87 offset:0x1600
	ds_read_b64_tr_b16 v[94:95], v87 offset:0x1e00
	v_add_u32_e32 v0, s100, v161
	ds_read_b128 v[186:189], v0
	ds_read_b128 v[190:193], v0 offset:8192
	v_mfma_f32_32x32x16_bf16 v[64:79], v[170:173], v[2:5], v[64:79]
	v_exp_f32_e32 v120, v120
	v_exp_f32_e32 v121, v121
	v_mfma_f32_32x32x16_bf16 v[48:63], v[174:177], v[2:5], v[48:63]
	v_exp_f32_e32 v122, v122
	v_exp_f32_e32 v123, v123
	v_mfma_f32_32x32x16_bf16 v[32:47], v[178:181], v[2:5], v[32:47]
	v_exp_f32_e32 v124, v124
	v_exp_f32_e32 v125, v125
	v_mfma_f32_32x32x16_bf16 v[16:31], v[182:185], v[2:5], v[16:31]
	v_exp_f32_e32 v126, v126
	v_exp_f32_e32 v127, v127
	v_cvt_pk_bf16_f32 v6, v120, v121
	v_cvt_pk_bf16_f32 v7, v122, v123
	v_cvt_pk_bf16_f32 v8, v124, v125
	v_cvt_pk_bf16_f32 v9, v126, v127
	v_add_f32_e32 v81, v120, v121
	v_add_f32_e32 v82, v122, v123
	v_add_f32_e32 v83, v124, v125
	v_add_f32_e32 v84, v126, v127
	v_add_f32_e32 v81, v81, v82
	v_add_f32_e32 v83, v83, v84
	v_add_f32_e32 v81, v81, v83
	v_add_f32_e32 v80, v80, v81
	s_waitcnt lgkmcnt(0)
	ds_read_b64_tr_b16 v[170:171], v87 offset:0x2000
	ds_read_b64_tr_b16 v[172:173], v87 offset:0x2800
	ds_read_b64_tr_b16 v[174:175], v87 offset:0x2200
	ds_read_b64_tr_b16 v[176:177], v87 offset:0x2a00
	ds_read_b64_tr_b16 v[178:179], v87 offset:0x2400
	ds_read_b64_tr_b16 v[180:181], v87 offset:0x2c00
	ds_read_b64_tr_b16 v[182:183], v87 offset:0x2600
	ds_read_b64_tr_b16 v[184:185], v87 offset:0x2e00
	v_add_u32_e32 v0, s100, v162
	ds_read_b128 v[202:205], v0
	ds_read_b128 v[206:209], v0 offset:8192
	v_mfma_f32_32x32x16_bf16 v[64:79], v[112:115], v[6:9], v[64:79]
	v_exp_f32_e32 v96, v96
	v_exp_f32_e32 v97, v97
	v_mfma_f32_32x32x16_bf16 v[48:63], v[116:119], v[6:9], v[48:63]
	v_exp_f32_e32 v98, v98
	v_exp_f32_e32 v99, v99
	v_mfma_f32_32x32x16_bf16 v[32:47], v[88:91], v[6:9], v[32:47]
	v_exp_f32_e32 v100, v100
	v_exp_f32_e32 v101, v101
	v_mfma_f32_32x32x16_bf16 v[16:31], v[92:95], v[6:9], v[16:31]
	v_exp_f32_e32 v102, v102
	v_exp_f32_e32 v103, v103
	v_cvt_pk_bf16_f32 v10, v96, v97
	v_cvt_pk_bf16_f32 v11, v98, v99
	v_cvt_pk_bf16_f32 v12, v100, v101
	v_cvt_pk_bf16_f32 v13, v102, v103
	v_add_f32_e32 v81, v96, v97
	v_add_f32_e32 v82, v98, v99
	v_add_f32_e32 v83, v100, v101
	v_add_f32_e32 v84, v102, v103
	v_add_f32_e32 v81, v81, v82
	v_add_f32_e32 v83, v83, v84
	v_add_f32_e32 v81, v81, v83
	v_add_f32_e32 v80, v80, v81
	s_waitcnt lgkmcnt(0)
	ds_read_b64_tr_b16 v[112:113], v87 offset:0x3000
	ds_read_b64_tr_b16 v[114:115], v87 offset:0x3800
	ds_read_b64_tr_b16 v[116:117], v87 offset:0x3200
	ds_read_b64_tr_b16 v[118:119], v87 offset:0x3a00
	ds_read_b64_tr_b16 v[88:89], v87 offset:0x3400
	ds_read_b64_tr_b16 v[90:91], v87 offset:0x3c00
	ds_read_b64_tr_b16 v[92:93], v87 offset:0x3600
	ds_read_b64_tr_b16 v[94:95], v87 offset:0x3e00
	v_add_u32_e32 v0, s100, v163
	ds_read_b128 v[210:213], v0
	ds_read_b128 v[214:217], v0 offset:8192
	v_mfma_f32_32x32x16_bf16 v[64:79], v[170:173], v[10:13], v[64:79]
	v_exp_f32_e32 v104, v104
	v_exp_f32_e32 v105, v105
	v_mfma_f32_32x32x16_bf16 v[48:63], v[174:177], v[10:13], v[48:63]
	v_exp_f32_e32 v106, v106
	v_exp_f32_e32 v107, v107
	v_mfma_f32_32x32x16_bf16 v[32:47], v[178:181], v[10:13], v[32:47]
	v_exp_f32_e32 v108, v108
	v_exp_f32_e32 v109, v109
	v_mfma_f32_32x32x16_bf16 v[16:31], v[182:185], v[10:13], v[16:31]
	v_exp_f32_e32 v110, v110
	v_exp_f32_e32 v111, v111
	v_cvt_pk_bf16_f32 v166, v104, v105
	v_cvt_pk_bf16_f32 v167, v106, v107
	v_cvt_pk_bf16_f32 v168, v108, v109
	v_cvt_pk_bf16_f32 v169, v110, v111
	v_add_f32_e32 v81, v104, v105
	v_add_f32_e32 v82, v106, v107
	v_add_f32_e32 v83, v108, v109
	v_add_f32_e32 v84, v110, v111
	v_add_f32_e32 v81, v81, v82
	v_add_f32_e32 v83, v83, v84
	v_add_f32_e32 v81, v81, v83
	v_add_f32_e32 v80, v80, v81
	s_waitcnt lgkmcnt(0)
	v_add_u32_e32 v0, s100, v164
	ds_read_b128 v[218:221], v0
	ds_read_b128 v[222:225], v0 offset:8192
	v_mfma_f32_32x32x16_bf16 v[64:79], v[112:115], v[166:169], v[64:79]
	v_mfma_f32_32x32x16_bf16 v[48:63], v[116:119], v[166:169], v[48:63]
	v_mfma_f32_32x32x16_bf16 v[32:47], v[88:91], v[166:169], v[32:47]
	v_mfma_f32_32x32x16_bf16 v[16:31], v[92:95], v[166:169], v[16:31]
	s_add_i32 s101, s48, 64
	s_cmp_le_u32 s101, s88
	s_cselect_b64 vcc, -1, 0
	v_cndmask_b32_e32 v2, 0, v158, vcc
	v_sub_f32_e32 v96, v2, v165
	v_mov_b32_e32 v97, v96
	v_mov_b32_e32 v98, v96
	v_mov_b32_e32 v99, v96
	v_mov_b32_e32 v100, v96
	v_mov_b32_e32 v101, v96
	v_mov_b32_e32 v102, v96
	v_mov_b32_e32 v103, v96
	v_mov_b32_e32 v104, v96
	v_mov_b32_e32 v105, v96
	v_mov_b32_e32 v106, v96
	v_mov_b32_e32 v107, v96
	v_mov_b32_e32 v108, v96
	v_mov_b32_e32 v109, v96
	v_mov_b32_e32 v110, v96
	v_mov_b32_e32 v111, v96
	s_waitcnt lgkmcnt(0)
	s_nop 0
	v_mfma_f32_32x32x16_bf16 v[112:127], v[186:189], v[128:131], v[96:111]
	v_mfma_f32_32x32x16_bf16 v[96:111], v[190:193], v[128:131], v[96:111]
	v_mfma_f32_32x32x16_bf16 v[112:127], v[202:205], v[132:135], v[112:127]
	v_mfma_f32_32x32x16_bf16 v[96:111], v[206:209], v[132:135], v[96:111]
	v_mfma_f32_32x32x16_bf16 v[112:127], v[210:213], v[136:139], v[112:127]
	v_mfma_f32_32x32x16_bf16 v[96:111], v[214:217], v[136:139], v[96:111]
	v_mfma_f32_32x32x16_bf16 v[112:127], v[218:221], v[140:143], v[112:127]
	v_mfma_f32_32x32x16_bf16 v[96:111], v[222:225], v[140:143], v[96:111]
	s_mov_b64 s[38:39], 0
	s_mov_b64 s[58:59], -1
	s_and_b64 vcc, exec, s[40:41]
	s_cbranch_vccz .LBB0_790

; #define LAS __attribute__((address_space(3)))
; #define MFMA32(a, b, c) __builtin_amdgcn_mfma_f32_32x32x16_bf16((a), (b), (c), 0, 0, 0)
; DI int at_v_rd_base(int lane) { return ((lane & 3) << 3) | (((lane >> 2) & 3) << 6) | (((lane >> 4) & 1) << 5) | (((lane >> 5) & 1) << 8); }
;     __device__ __forceinline__ void init(const void* A_, const void* B_, int lda_, int ldb_, int M, unsigned mask_, int G_, int c_) { A = (const char*)A_; B = (const char*)B_; lda = lda_; ldb = ldb_; nM = M / BM; mask = mask_; nN = __builtin_popcount(mask_); nwg = nM * nN; G = G_; c = c_; }
; template <int KS> DI void at_qk(f32x16& p0, f32x16& p1, LAS const unsigned char* Kt, int mapB, const bf16x8 (&qr)[8], float init, int r32, int hi) {
; #pragma unroll
;     for (int i = 0; i < 16; ++i) { p0[i] = init; p1[i] = init; }
;     bf16x8 kb[KS][2];
; #pragma unroll
;     for (int d0 = 0; d0 < KS; ++d0) { const int cb = mapB + (d0 * 16 + hi * 8) * 2;
;         kb[d0][0] = *(const LAS bf16x8*)(Kt + AT_KSWZ(r32, cb)); kb[d0][1] = *(const LAS bf16x8*)(Kt + AT_KSWZ(32 + r32, cb)); }
;     __builtin_amdgcn_sched_barrier(0);
; #pragma unroll
;     for (int d0 = 0; d0 < KS; ++d0) { p0 = MFMA32(kb[d0][0], qr[d0], p0); p1 = MFMA32(kb[d0][1], qr[d0], p1); }
; DI void attn_unit_diff(const Ctx& C, int l, int b, int h, int j) {
;     ...
;     f32x16 o[4], ol = {}; float m_run = 0.f; bool first = true;
; #pragma unroll
;     for (int d0 = 0; d0 < 4; ++d0) o[d0] = f32x16{};
;     const bf16x8 ones = {16256, 16256, 16256, 16256, 16256, 16256, 16256, 16256};
;     asm volatile("s_waitcnt vmcnt(0) lgkmcnt(0)\n\ts_barrier" ::: "memory");
;     const float cfar = tabl[0];
;     const int vrd = at_v_rd_base(lane);
;     for (int sd = 0; sd < nt; ++sd) {
;         const int slot = sd % 3;
;         const bool staged = sd + 2 < nt;
;         if (staged) at_stage1(C.lds, projb, kcolB, vcolB, sd + 2, (sd + 2) % 3, wid, lb0, lb1);
;         if (sd <= cw) {
;             LAS const unsigned char* Kt = C.lds + slot * 32768;
;             const int vb = (int)(size_t)(Kt + 16384) + vrd;
;             const bool nearb = (sd * 64 + 63 - q0w) > -305;
;             LAS const float* tabp = tabl + (sd * 64 - qpos + TABB_OFF + 4 * hi);
;             f32x16 p0, p1;
;             at_qk<KS>(p0, p1, Kt, g * 128, qr, (nearb ? 0.f : cfar) - m_run, r32, hi);
.LBB0_828:
	s_or_b64 exec, exec, s[58:59]
	s_and_b32 s11, s22, 15
	s_waitcnt vmcnt(0) lgkmcnt(0)
	s_barrier
	v_mov_b32_e32 v4, s50
	s_lshl_b32 s6, s6, 1
	v_readlane_b32 s7, v252, 22
	s_lshl_b32 s31, s11, 7
	s_lshl_b32 s11, s11, 16
	s_waitcnt lgkmcnt(0)
	ds_read_b32 v158, v4
	v_and_b32_e32 v4, 24, v8
	v_and_b32_e32 v7, 0x100, v8
	v_lshlrev_b32_e32 v8, 4, v156
	v_readlane_b32 s15, v252, 26
	v_readlane_b32 s35, v252, 23
	v_mov_b32_e32 v3, v1
	s_or_b32 s7, s6, s7
	s_add_i32 s11, s11, 0x10000
	v_lshlrev_b32_e32 v145, 4, v154
	v_add_u32_e32 v9, s15, v8
	v_lshlrev_b32_e32 v11, 4, v155
	v_lshlrev_b32_e32 v15, 2, v154
	s_add_i32 s16, s55, 0xfffffe90
	s_or_b32 s31, s35, s31
	s_add_i32 s52, s48, s28
	v_and_b32_e32 v5, 0xc0, v145
	v_lshlrev_b32_e32 v6, 1, v154
	v_lshlrev_b32_e32 v10, 8, v155
	v_and_b32_e32 v11, 0x70, v11
	v_add_u32_e32 v14, 0x60, v9
	v_xor_b32_e32 v157, 0x80, v15
	v_add_lshl_u32 v15, s31, v155, 2
	v_lshl_add_u64 v[2:3], s[42:43], 0, v[2:3]
	s_add_u32 s42, s96, s42
	v_and_b32_e32 v6, 32, v6
	v_add_u32_e32 v12, 32, v9
	v_add_u32_e32 v13, 64, v9
	v_sub_u32_e32 v159, v8, v15
	v_add3_u32 v5, v7, s91, v5
	v_xad_u32 v164, v14, v11, v10
	s_addc_u32 s43, s89, s43
	v_mov_b32_e32 v14, v1
	v_mov_b32_e32 v15, v1
	v_add3_u32 v160, v5, v6, v4
	v_xad_u32 v161, v9, v11, v10
	v_xad_u32 v162, v12, v11, v10
	v_xad_u32 v163, v13, v11, v10
	v_lshl_add_u64 v[146:147], s[70:71], 0, v[2:3]
	v_lshl_add_u64 v[148:149], s[72:73], 0, v[2:3]
	v_lshl_add_u64 v[150:151], s[42:43], 0, v[0:1]
	v_mov_b32_e32 v0, v1
	v_mov_b32_e32 v2, v1
	v_mov_b32_e32 v3, v1
	v_mov_b32_e32 v4, v1
	v_mov_b32_e32 v5, v1
	v_mov_b32_e32 v6, v1
	v_mov_b32_e32 v7, v1
	v_mov_b32_e32 v8, v1
	v_mov_b32_e32 v9, v1
	v_mov_b32_e32 v10, v1
	v_mov_b32_e32 v11, v1
	v_mov_b32_e32 v12, v1
	v_mov_b32_e32 v13, v1
	v_mov_b64_e32 v[78:79], v[14:15]
	v_mov_b64_e32 v[62:63], v[14:15]
	v_mov_b64_e32 v[46:47], v[14:15]
	v_mov_b64_e32 v[30:31], v[14:15]
	v_mov_b64_e32 v[94:95], v[14:15]
	s_mov_b32 s15, 2
	s_mov_b32 s28, 0
	v_mov_b32_e32 v165, 0
	s_mov_b64 s[42:43], -1
	s_mov_b32 s31, 0
	v_mov_b64_e32 v[76:77], v[12:13]
	v_mov_b64_e32 v[74:75], v[10:11]
	v_mov_b64_e32 v[72:73], v[8:9]
	v_mov_b64_e32 v[70:71], v[6:7]
	v_mov_b64_e32 v[68:69], v[4:5]
	v_mov_b64_e32 v[66:67], v[2:3]
	v_mov_b64_e32 v[64:65], v[0:1]
	v_mov_b64_e32 v[60:61], v[12:13]
	v_mov_b64_e32 v[58:59], v[10:11]
	v_mov_b64_e32 v[56:57], v[8:9]
	v_mov_b64_e32 v[54:55], v[6:7]
	v_mov_b64_e32 v[52:53], v[4:5]
	v_mov_b64_e32 v[50:51], v[2:3]
	v_mov_b64_e32 v[48:49], v[0:1]
	v_mov_b64_e32 v[44:45], v[12:13]
	v_mov_b64_e32 v[42:43], v[10:11]
	v_mov_b64_e32 v[40:41], v[8:9]
	v_mov_b64_e32 v[38:39], v[6:7]
	v_mov_b64_e32 v[36:37], v[4:5]
	v_mov_b64_e32 v[34:35], v[2:3]
	v_mov_b64_e32 v[32:33], v[0:1]
	v_mov_b64_e32 v[28:29], v[12:13]
	v_mov_b64_e32 v[26:27], v[10:11]
	v_mov_b64_e32 v[24:25], v[8:9]
	v_mov_b64_e32 v[22:23], v[6:7]
	v_mov_b64_e32 v[20:21], v[4:5]
	v_mov_b64_e32 v[18:19], v[2:3]
	v_mov_b64_e32 v[16:17], v[0:1]
	v_mov_b64_e32 v[92:93], v[12:13]
	v_mov_b64_e32 v[90:91], v[10:11]
	v_mov_b64_e32 v[88:89], v[8:9]
	v_mov_b64_e32 v[86:87], v[6:7]
	v_mov_b64_e32 v[84:85], v[4:5]
	v_mov_b64_e32 v[82:83], v[2:3]
	v_mov_b64_e32 v[80:81], v[0:1]
	s_mov_b32 s35, 0
	s_waitcnt vmcnt(0)
	s_mul_hi_u32 s48, s15, 0xaaaaaaab
	s_lshr_b32 s48, s48, 1
	s_mul_i32 s48, s48, 0x18000
	s_sub_i32 s49, s60, s48
	s_sub_i32 s57, s61, s48
	s_add_i32 s49, s31, s49
	v_lshl_add_u64 v[2:3], v[150:151], 0, s[52:53]
	s_sub_i32 s58, s4, s48
	s_add_i32 m0, s90, s49
	v_lshl_add_u64 v[4:5], v[2:3], 0, s[36:37]
	s_add_i32 s49, s31, s57
	s_sub_i32 s48, s5, s48
	global_load_lds_dwordx4 v[4:5], off
	v_lshl_add_u64 v[4:5], v[148:149], 0, s[52:53]
	s_add_i32 m0, s90, s49
	s_add_i32 s49, s31, s58
	global_load_lds_dwordx4 v[4:5], off
	v_lshl_add_u64 v[2:3], v[2:3], 0, s[24:25]
	s_add_i32 m0, s90, s49
	s_add_i32 s48, s31, s48
	global_load_lds_dwordx4 v[2:3], off
	v_lshl_add_u64 v[2:3], v[146:147], 0, s[52:53]
	s_add_i32 m0, s90, s48
	s_nop 0
	global_load_lds_dwordx4 v[2:3], off
	v_lshl_add_u64 v[146:147], v[146:147], 0, s[68:69]
	v_lshl_add_u64 v[148:149], v[148:149], 0, s[68:69]
	v_lshl_add_u64 v[150:151], v[150:151], 0, s[68:69]
	ds_read_b128 v[186:189], v161
	ds_read_b128 v[190:193], v161 offset:8192
	ds_read_b128 v[202:205], v162
	ds_read_b128 v[206:209], v162 offset:8192
	ds_read_b128 v[210:213], v163
	ds_read_b128 v[214:217], v163 offset:8192
	ds_read_b128 v[218:221], v164
	ds_read_b128 v[222:225], v164 offset:8192
	s_cmp_le_i32 s28, s16
	s_cselect_b64 vcc, -1, 0
	s_waitcnt lgkmcnt(0)
	v_cndmask_b32_e32 v2, 0, v158, vcc
	v_sub_f32_e32 v96, v2, v165
	v_mov_b32_e32 v97, v96
	v_mov_b32_e32 v98, v96
	v_mov_b32_e32 v99, v96
	v_mov_b32_e32 v100, v96
	v_mov_b32_e32 v101, v96
	v_mov_b32_e32 v102, v96
	v_mov_b32_e32 v103, v96
	v_mov_b32_e32 v104, v96
	v_mov_b32_e32 v105, v96
	v_mov_b32_e32 v106, v96
	v_mov_b32_e32 v107, v96
	v_mov_b32_e32 v108, v96
	v_mov_b32_e32 v109, v96
	v_mov_b32_e32 v110, v96
	v_mov_b32_e32 v111, v96
	s_waitcnt lgkmcnt(0)
	s_nop 0
	v_mfma_f32_32x32x16_bf16 v[112:127], v[186:189], v[128:131], v[96:111]
	v_mfma_f32_32x32x16_bf16 v[96:111], v[190:193], v[128:131], v[96:111]
	v_mfma_f32_32x32x16_bf16 v[112:127], v[202:205], v[132:135], v[112:127]
	v_mfma_f32_32x32x16_bf16 v[96:111], v[206:209], v[132:135], v[96:111]
	v_mfma_f32_32x32x16_bf16 v[112:127], v[210:213], v[136:139], v[112:127]
	v_mfma_f32_32x32x16_bf16 v[96:111], v[214:217], v[136:139], v[96:111]
	v_mfma_f32_32x32x16_bf16 v[112:127], v[218:221], v[140:143], v[112:127]
	v_mfma_f32_32x32x16_bf16 v[96:111], v[222:225], v[140:143], v[96:111]
	s_branch .LBB0_830

; #define LAS __attribute__((address_space(3)))
; DI float at_softmax(f32x16& p0, f32x16& p1, float& m_run, bool first, bool nearb, LAS const float* tabp, int lane) {
;     if (nearb) {
; #pragma unroll
;         for (int i = 0; i < 16; ++i) { p0[i] += tabp[8 * (i >> 2) + (i & 3)]; p1[i] += tabp[32 + 8 * (i >> 2) + (i & 3)]; }
;     }
;     float mx = p0[0];
; #pragma unroll
;     for (int i = 1; i < 16; ++i) mx = fmaxf(mx, p0[i]);
; #pragma unroll
;     for (int i = 0; i < 16; ++i) mx = fmaxf(mx, p1[i]);
; DI void attn_unit_diff(const Ctx& C, int l, int b, int h, int j) {
;     ...
;         if (sd <= cw) {
;             LAS const unsigned char* Kt = C.lds + slot * 32768;
;             const int vb = (int)(size_t)(Kt + 16384) + vrd;
;             const bool nearb = (sd * 64 + 63 - q0w) > -305;
;             LAS const float* tabp = tabl + (sd * 64 - qpos + TABB_OFF + 4 * hi);
;             f32x16 p0, p1;
;             at_qk<KS>(p0, p1, Kt, g * 128, qr, (nearb ? 0.f : cfar) - m_run, r32, hi);
;             const float alpha = at_softmax(p0, p1, m_run, first, nearb, tabp, lane);
.LBB0_835:
	s_lshr_b32 s48, s35, 2
	s_lshl_b32 s48, s48, 17
	s_add_i32 s100, s35, 1
	s_and_b32 s100, s100, 3
	s_lshl_b32 s100, s100, 15
	s_add_i32 s49, s31, 0
	s_cmp_le_i32 s28, s16
	s_cselect_b64 vcc, -1, 0
	s_and_b64 vcc, exec, vcc
	s_cbranch_vccnz .LBB0_837
	v_add_u32_e32 v0, 0, v159
	v_add_u32_e32 v2, 0x207fc, v0
	v_add_u32_e32 v4, 0x2087c, v0
	ds_read2_b32 v[2:3], v2 offset1:1
	ds_read2_b32 v[4:5], v4 offset1:1
	v_add_u32_e32 v6, 0x20804, v0
	v_add_u32_e32 v8, 0x20884, v0
	v_add_u32_e32 v10, 0x2081c, v0
	v_add_u32_e32 v12, 0x2089c, v0
	v_add_u32_e32 v14, 0x20824, v0
	v_add_u32_e32 v166, 0x208a4, v0
	v_add_u32_e32 v168, 0x2083c, v0
	v_add_u32_e32 v170, 0x208bc, v0
	v_add_u32_e32 v172, 0x20844, v0
	v_add_u32_e32 v174, 0x208c4, v0
	v_add_u32_e32 v176, 0x2085c, v0
	v_add_u32_e32 v178, 0x208dc, v0
	v_add_u32_e32 v180, 0x20864, v0
	v_add_u32_e32 v0, 0x208e4, v0
	ds_read2_b32 v[6:7], v6 offset1:1
	ds_read2_b32 v[8:9], v8 offset1:1
	ds_read2_b32 v[10:11], v10 offset1:1
	ds_read2_b32 v[12:13], v12 offset1:1
	ds_read2_b32 v[14:15], v14 offset1:1
	ds_read2_b32 v[166:167], v166 offset1:1
	ds_read2_b32 v[168:169], v168 offset1:1
	ds_read2_b32 v[170:171], v170 offset1:1
	ds_read2_b32 v[172:173], v172 offset1:1
	ds_read2_b32 v[174:175], v174 offset1:1
	ds_read2_b32 v[176:177], v176 offset1:1
	ds_read2_b32 v[178:179], v178 offset1:1
	ds_read2_b32 v[180:181], v180 offset1:1
	s_waitcnt lgkmcnt(0)
	v_pk_add_f32 v[112:113], v[112:113], v[2:3]
	ds_read2_b32 v[2:3], v0 offset1:1
	v_pk_add_f32 v[124:125], v[124:125], v[176:177]
	v_pk_add_f32 v[122:123], v[122:123], v[172:173]
	v_pk_add_f32 v[126:127], v[126:127], v[180:181]
	v_pk_add_f32 v[120:121], v[120:121], v[168:169]
	v_pk_add_f32 v[118:119], v[118:119], v[14:15]
	v_pk_add_f32 v[116:117], v[116:117], v[10:11]
	v_pk_add_f32 v[114:115], v[114:115], v[6:7]
	s_waitcnt lgkmcnt(0)
	v_pk_add_f32 v[110:111], v[110:111], v[2:3]
	v_pk_add_f32 v[108:109], v[108:109], v[178:179]
	v_pk_add_f32 v[106:107], v[106:107], v[174:175]
	v_pk_add_f32 v[104:105], v[104:105], v[170:171]
	v_pk_add_f32 v[102:103], v[102:103], v[166:167]
	v_pk_add_f32 v[100:101], v[100:101], v[12:13]
	v_pk_add_f32 v[98:99], v[98:99], v[8:9]
	v_pk_add_f32 v[96:97], v[96:97], v[4:5]
.LBB0_837:
	s_nop 0
	v_max_f32_e32 v0, v113, v113
	v_max_f32_e32 v2, v112, v112
	v_max_f32_e32 v0, v2, v0
	v_max3_f32 v0, v0, v114, v115
	v_max3_f32 v0, v0, v116, v117
	v_max3_f32 v0, v0, v118, v119
	v_max3_f32 v0, v0, v120, v121
	v_max3_f32 v0, v0, v122, v123
	v_max3_f32 v0, v0, v124, v125
	v_max3_f32 v0, v0, v126, v127
	v_max3_f32 v0, v0, v96, v97
	v_max3_f32 v0, v0, v98, v99
	v_max3_f32 v0, v0, v100, v101
	v_max3_f32 v0, v0, v102, v103
	v_max3_f32 v0, v0, v104, v105
	v_max3_f32 v0, v0, v106, v107
	s_xor_b64 s[58:59], s[42:43], -1
	v_max3_f32 v0, v0, v108, v109
	v_max3_f32 v2, v0, v110, v111
	s_and_b64 vcc, exec, s[58:59]
	s_cbranch_vccz .LBB0_839
	s_mov_b32 s49, 0x41000000
	v_cmp_ge_f32_e32 vcc, s49, v2
	s_cmp_lg_u64 vcc, exec
	s_cselect_b64 s[58:59], -1, 0
	s_cbranch_execz .LBB0_840
	s_branch .LBB0_841

; #define MFMA32(a, b, c) __builtin_amdgcn_mfma_f32_32x32x16_bf16((a), (b), (c), 0, 0, 0)
; DI float at_softmax(f32x16& p0, f32x16& p1, float& m_run, bool first, bool nearb, LAS const float* tabp, int lane) {
;     ...
;     for (int i = 0; i < 16; ++i) p0[i] = __builtin_amdgcn_exp2f(p0[i]);
; #pragma unroll
;     for (int i = 0; i < 16; ++i) p1[i] = __builtin_amdgcn_exp2f(p1[i]);
;     return alpha;
; }
; DI bf16x8 at_pack(const f32x16& p, int s8) {
;     u32x4 w; w.x = at_cvtpk(p[s8], p[s8 + 1]); w.y = at_cvtpk(p[s8 + 2], p[s8 + 3]); w.z = at_cvtpk(p[s8 + 4], p[s8 + 5]); w.w = at_cvtpk(p[s8 + 6], p[s8 + 7]);
;     return __builtin_bit_cast(bf16x8, w);
; }
; template <int D0> DI void at_pv_block(f32x16 (&o)[4], int vb, const bf16x8 (&pf)[4]) {
;     const s16x4 l0 = at_tr_read<D0 * 512 + 0 * 4096>(vb), h0 = at_tr_read<D0 * 512 + 0 * 4096 + 2048>(vb), l1 = at_tr_read<D0 * 512 + 1 * 4096>(vb), h1 = at_tr_read<D0 * 512 + 1 * 4096 + 2048>(vb);
;     const s16x4 l2 = at_tr_read<D0 * 512 + 2 * 4096>(vb), h2 = at_tr_read<D0 * 512 + 2 * 4096 + 2048>(vb), l3 = at_tr_read<D0 * 512 + 3 * 4096>(vb), h3 = at_tr_read<D0 * 512 + 3 * 4096 + 2048>(vb);
;     asm volatile("s_waitcnt lgkmcnt(0)" ::: "memory"); __builtin_amdgcn_sched_barrier(0);
;     ...
;     o[D0] = MFMA32(AT_PK(l0, h0), pf[0], o[D0]); o[D0] = MFMA32(AT_PK(l1, h1), pf[1], o[D0]); o[D0] = MFMA32(AT_PK(l2, h2), pf[2], o[D0]); o[D0] = MFMA32(AT_PK(l3, h3), pf[3], o[D0]);
; DI void attn_unit_diff(const Ctx& C, int l, int b, int h, int j) {
;     ...
;             at_qk<KS>(p0, p1, Kt, g * 128, qr, (nearb ? 0.f : cfar) - m_run, r32, hi);
;             const float alpha = at_softmax(p0, p1, m_run, first, nearb, tabp, lane);
;             first = false;
;             if (__any(alpha != 1.f)) {
;                 ol[0] *= alpha;
; #pragma unroll
;                 for (int d0 = 0; d0 < 4; ++d0)
; #pragma unroll
;                     for (int i = 0; i < 16; ++i) o[d0][i] *= alpha;
;             }
;             bf16x8 pf[4];
;             pf[0] = at_pack(p0, 0); pf[1] = at_pack(p0, 8); pf[2] = at_pack(p1, 0); pf[3] = at_pack(p1, 8);
;             ol = MFMA32(ones, pf[0], ol); ol = MFMA32(ones, pf[1], ol); ol = MFMA32(ones, pf[2], ol); ol = MFMA32(ones, pf[3], ol);
;             at_pv_block<0>(o, vb, pf); at_pv_block<1>(o, vb, pf); at_pv_block<2>(o, vb, pf); at_pv_block<3>(o, vb, pf);
.LBB0_844:
	v_subrev_u32_e32 v87, s48, v160
	v_add_u32_e32 v87, s31, v87
	ds_read_b64_tr_b16 v[170:171], v87 offset:0x0
	ds_read_b64_tr_b16 v[172:173], v87 offset:0x800
	ds_read_b64_tr_b16 v[174:175], v87 offset:0x200
	ds_read_b64_tr_b16 v[176:177], v87 offset:0xa00
	ds_read_b64_tr_b16 v[178:179], v87 offset:0x400
	ds_read_b64_tr_b16 v[180:181], v87 offset:0xc00
	ds_read_b64_tr_b16 v[182:183], v87 offset:0x600
	ds_read_b64_tr_b16 v[184:185], v87 offset:0xe00
	v_exp_f32_e32 v112, v112
	v_exp_f32_e32 v113, v113
	v_exp_f32_e32 v114, v114
	v_exp_f32_e32 v115, v115
	v_exp_f32_e32 v116, v116
	v_exp_f32_e32 v117, v117
	v_exp_f32_e32 v118, v118
	v_exp_f32_e32 v119, v119
	v_cvt_pk_bf16_f32 v2, v112, v113
	v_cvt_pk_bf16_f32 v3, v114, v115
	v_cvt_pk_bf16_f32 v4, v116, v117
	v_cvt_pk_bf16_f32 v5, v118, v119
	v_add_f32_e32 v81, v112, v113
	v_add_f32_e32 v82, v114, v115
	v_add_f32_e32 v83, v116, v117
	v_add_f32_e32 v84, v118, v119
	v_add_f32_e32 v81, v81, v82
	v_add_f32_e32 v83, v83, v84
	v_add_f32_e32 v81, v81, v83
	v_add_f32_e32 v80, v80, v81
	s_waitcnt lgkmcnt(0)
	ds_read_b64_tr_b16 v[112:113], v87 offset:0x1000
	ds_read_b64_tr_b16 v[114:115], v87 offset:0x1800
	ds_read_b64_tr_b16 v[116:117], v87 offset:0x1200
	ds_read_b64_tr_b16 v[118:119], v87 offset:0x1a00
	ds_read_b64_tr_b16 v[88:89], v87 offset:0x1400
	ds_read_b64_tr_b16 v[90:91], v87 offset:0x1c00
	ds_read_b64_tr_b16 v[92:93], v87 offset:0x1600
	ds_read_b64_tr_b16 v[94:95], v87 offset:0x1e00
	v_add_u32_e32 v0, s100, v161
	ds_read_b128 v[186:189], v0
	ds_read_b128 v[190:193], v0 offset:8192
	v_mfma_f32_32x32x16_bf16 v[64:79], v[170:173], v[2:5], v[64:79]
	v_exp_f32_e32 v120, v120
	v_exp_f32_e32 v121, v121
	v_mfma_f32_32x32x16_bf16 v[48:63], v[174:177], v[2:5], v[48:63]
	v_exp_f32_e32 v122, v122
	v_exp_f32_e32 v123, v123
	v_mfma_f32_32x32x16_bf16 v[32:47], v[178:181], v[2:5], v[32:47]
	v_exp_f32_e32 v124, v124
	v_exp_f32_e32 v125, v125
	v_mfma_f32_32x32x16_bf16 v[16:31], v[182:185], v[2:5], v[16:31]
	v_exp_f32_e32 v126, v126
	v_exp_f32_e32 v127, v127
	v_cvt_pk_bf16_f32 v6, v120, v121
	v_cvt_pk_bf16_f32 v7, v122, v123
	v_cvt_pk_bf16_f32 v8, v124, v125
	v_cvt_pk_bf16_f32 v9, v126, v127
	v_add_f32_e32 v81, v120, v121
	v_add_f32_e32 v82, v122, v123
	v_add_f32_e32 v83, v124, v125
	v_add_f32_e32 v84, v126, v127
	v_add_f32_e32 v81, v81, v82
	v_add_f32_e32 v83, v83, v84
	v_add_f32_e32 v81, v81, v83
	v_add_f32_e32 v80, v80, v81
	s_waitcnt lgkmcnt(0)
	ds_read_b64_tr_b16 v[170:171], v87 offset:0x2000
	ds_read_b64_tr_b16 v[172:173], v87 offset:0x2800
	ds_read_b64_tr_b16 v[174:175], v87 offset:0x2200
	ds_read_b64_tr_b16 v[176:177], v87 offset:0x2a00
	ds_read_b64_tr_b16 v[178:179], v87 offset:0x2400
	ds_read_b64_tr_b16 v[180:181], v87 offset:0x2c00
	ds_read_b64_tr_b16 v[182:183], v87 offset:0x2600
	ds_read_b64_tr_b16 v[184:185], v87 offset:0x2e00
	v_add_u32_e32 v0, s100, v162
	ds_read_b128 v[202:205], v0
	ds_read_b128 v[206:209], v0 offset:8192
	v_mfma_f32_32x32x16_bf16 v[64:79], v[112:115], v[6:9], v[64:79]
	v_exp_f32_e32 v96, v96
	v_exp_f32_e32 v97, v97
	v_mfma_f32_32x32x16_bf16 v[48:63], v[116:119], v[6:9], v[48:63]
	v_exp_f32_e32 v98, v98
	v_exp_f32_e32 v99, v99
	v_mfma_f32_32x32x16_bf16 v[32:47], v[88:91], v[6:9], v[32:47]
	v_exp_f32_e32 v100, v100
	v_exp_f32_e32 v101, v101
	v_mfma_f32_32x32x16_bf16 v[16:31], v[92:95], v[6:9], v[16:31]
	v_exp_f32_e32 v102, v102
	v_exp_f32_e32 v103, v103
	v_cvt_pk_bf16_f32 v10, v96, v97
	v_cvt_pk_bf16_f32 v11, v98, v99
	v_cvt_pk_bf16_f32 v12, v100, v101
	v_cvt_pk_bf16_f32 v13, v102, v103
	v_add_f32_e32 v81, v96, v97
	v_add_f32_e32 v82, v98, v99
	v_add_f32_e32 v83, v100, v101
	v_add_f32_e32 v84, v102, v103
	v_add_f32_e32 v81, v81, v82
	v_add_f32_e32 v83, v83, v84
	v_add_f32_e32 v81, v81, v83
	v_add_f32_e32 v80, v80, v81
	s_waitcnt lgkmcnt(0)
	ds_read_b64_tr_b16 v[112:113], v87 offset:0x3000
	ds_read_b64_tr_b16 v[114:115], v87 offset:0x3800
	ds_read_b64_tr_b16 v[116:117], v87 offset:0x3200
	ds_read_b64_tr_b16 v[118:119], v87 offset:0x3a00
	ds_read_b64_tr_b16 v[88:89], v87 offset:0x3400
	ds_read_b64_tr_b16 v[90:91], v87 offset:0x3c00
	ds_read_b64_tr_b16 v[92:93], v87 offset:0x3600
	ds_read_b64_tr_b16 v[94:95], v87 offset:0x3e00
	v_add_u32_e32 v0, s100, v163
	ds_read_b128 v[210:213], v0
	ds_read_b128 v[214:217], v0 offset:8192
	v_mfma_f32_32x32x16_bf16 v[64:79], v[170:173], v[10:13], v[64:79]
	v_exp_f32_e32 v104, v104
	v_exp_f32_e32 v105, v105
	v_mfma_f32_32x32x16_bf16 v[48:63], v[174:177], v[10:13], v[48:63]
	v_exp_f32_e32 v106, v106
	v_exp_f32_e32 v107, v107
	v_mfma_f32_32x32x16_bf16 v[32:47], v[178:181], v[10:13], v[32:47]
	v_exp_f32_e32 v108, v108
	v_exp_f32_e32 v109, v109
	v_mfma_f32_32x32x16_bf16 v[16:31], v[182:185], v[10:13], v[16:31]
	v_exp_f32_e32 v110, v110
	v_exp_f32_e32 v111, v111
	v_cvt_pk_bf16_f32 v166, v104, v105
	v_cvt_pk_bf16_f32 v167, v106, v107
	v_cvt_pk_bf16_f32 v168, v108, v109
	v_cvt_pk_bf16_f32 v169, v110, v111
	v_add_f32_e32 v81, v104, v105
	v_add_f32_e32 v82, v106, v107
	v_add_f32_e32 v83, v108, v109
	v_add_f32_e32 v84, v110, v111
	v_add_f32_e32 v81, v81, v82
	v_add_f32_e32 v83, v83, v84
	v_add_f32_e32 v81, v81, v83
	v_add_f32_e32 v80, v80, v81
	s_waitcnt lgkmcnt(0)
	v_add_u32_e32 v0, s100, v164
	ds_read_b128 v[218:221], v0
	ds_read_b128 v[222:225], v0 offset:8192
	v_mfma_f32_32x32x16_bf16 v[64:79], v[112:115], v[166:169], v[64:79]
	v_mfma_f32_32x32x16_bf16 v[48:63], v[116:119], v[166:169], v[48:63]
	v_mfma_f32_32x32x16_bf16 v[32:47], v[88:91], v[166:169], v[32:47]
	v_mfma_f32_32x32x16_bf16 v[16:31], v[92:95], v[166:169], v[16:31]
	s_add_i32 s101, s28, 64
	s_cmp_le_i32 s101, s16
	s_cselect_b64 vcc, -1, 0
	v_cndmask_b32_e32 v2, 0, v158, vcc
	v_sub_f32_e32 v96, v2, v165
	v_mov_b32_e32 v97, v96
	v_mov_b32_e32 v98, v96
	v_mov_b32_e32 v99, v96
	v_mov_b32_e32 v100, v96
	v_mov_b32_e32 v101, v96
	v_mov_b32_e32 v102, v96
	v_mov_b32_e32 v103, v96
	v_mov_b32_e32 v104, v96
	v_mov_b32_e32 v105, v96
	v_mov_b32_e32 v106, v96
	v_mov_b32_e32 v107, v96
	v_mov_b32_e32 v108, v96
	v_mov_b32_e32 v109, v96
	v_mov_b32_e32 v110, v96
	v_mov_b32_e32 v111, v96
	s_waitcnt lgkmcnt(0)
	s_nop 0
	v_mfma_f32_32x32x16_bf16 v[112:127], v[186:189], v[128:131], v[96:111]
	v_mfma_f32_32x32x16_bf16 v[96:111], v[190:193], v[128:131], v[96:111]
	v_mfma_f32_32x32x16_bf16 v[112:127], v[202:205], v[132:135], v[112:127]
	v_mfma_f32_32x32x16_bf16 v[96:111], v[206:209], v[132:135], v[96:111]
	v_mfma_f32_32x32x16_bf16 v[112:127], v[210:213], v[136:139], v[112:127]
	v_mfma_f32_32x32x16_bf16 v[96:111], v[214:217], v[136:139], v[96:111]
	v_mfma_f32_32x32x16_bf16 v[112:127], v[218:221], v[140:143], v[112:127]
	v_mfma_f32_32x32x16_bf16 v[96:111], v[222:225], v[140:143], v[96:111]
	s_mov_b64 s[42:43], 0
	s_mov_b64 s[58:59], -1
	s_and_b64 vcc, exec, s[76:77]
	s_cbranch_vccz .LBB0_833
